# v44 + prologue: b1f loop 4 round trips instead of 16, first-norm rows prefetched
# baseline (speedup 1.0000x reference)
; __device__ __forceinline__ void prologue(const Ctx& C, const In& I, unsigned char* ws, bf16* hs0) {
;     ...
;     for (int w = C.ngw - 1 - C.gw; w < 256; w += C.ngw) {
;         const int e0 = 4 * w, jk = e0 >> 8, col = (e0 & 255) + (C.lane & 3), ks = C.lane >> 2;
;         const float* pe = I.nsa_pe + (size_t)jk * 2048 + 128 * ks; const float* w1 = I.nsa_w1 + (size_t)jk * 2048 * 256 + (size_t)(128 * ks) * 256 + col; float sacc = 0.f;
; #pragma unroll 8
;         for (int i = 0; i < 128; ++i) sacc += pe[i] * w1[(size_t)i * 256];
;         sacc += __shfl_xor(sacc, 4); sacc += __shfl_xor(sacc, 8); sacc += __shfl_xor(sacc, 16); sacc += __shfl_xor(sacc, 32);
;         if (C.lane < 4) b1f[e0 + C.lane] = sacc + I.nsa_b1[e0 + C.lane];
.LBB0_81:
	v_lshl_add_u64 v[20:21], v[6:7], 0, s[12:13]
	s_add_u32 s12, s12, 0x80
	s_addc_u32 s13, s13, 0
	global_load_dwordx4 v[64:67], v[20:21], off offset:0
	global_load_dwordx4 v[68:71], v[20:21], off offset:16
	v_add_co_u32_e32 v24, vcc, 0xfffff000, v8
	s_nop 1
	v_addc_co_u32_e32 v25, vcc, -1, v9, vcc
	global_load_dword v72, v[24:25], off offset:-3072
	global_load_dword v73, v[24:25], off offset:-2048
	global_load_dword v74, v[24:25], off offset:-1024
	global_load_dword v75, v[8:9], off offset:-4096
	global_load_dword v76, v[8:9], off offset:-3072
	global_load_dword v77, v[8:9], off offset:-2048
	global_load_dword v78, v[8:9], off offset:-1024
	global_load_dword v79, v[8:9], off
	v_lshl_add_u64 v[128:129], v[8:9], 0, s[10:11]
	global_load_dwordx4 v[80:83], v[20:21], off offset:32
	global_load_dwordx4 v[84:87], v[20:21], off offset:48
	v_add_co_u32_e32 v134, vcc, 0xfffff000, v128
	s_nop 1
	v_addc_co_u32_e32 v135, vcc, -1, v129, vcc
	global_load_dword v88, v[134:135], off offset:-3072
	global_load_dword v89, v[134:135], off offset:-2048
	global_load_dword v90, v[134:135], off offset:-1024
	global_load_dword v91, v[128:129], off offset:-4096
	global_load_dword v92, v[128:129], off offset:-3072
	global_load_dword v93, v[128:129], off offset:-2048
	global_load_dword v94, v[128:129], off offset:-1024
	global_load_dword v95, v[128:129], off
	v_lshl_add_u64 v[130:131], v[128:129], 0, s[10:11]
	global_load_dwordx4 v[96:99], v[20:21], off offset:64
	global_load_dwordx4 v[100:103], v[20:21], off offset:80
	v_add_co_u32_e32 v136, vcc, 0xfffff000, v130
	s_nop 1
	v_addc_co_u32_e32 v137, vcc, -1, v131, vcc
	global_load_dword v104, v[136:137], off offset:-3072
	global_load_dword v105, v[136:137], off offset:-2048
	global_load_dword v106, v[136:137], off offset:-1024
	global_load_dword v107, v[130:131], off offset:-4096
	global_load_dword v108, v[130:131], off offset:-3072
	global_load_dword v109, v[130:131], off offset:-2048
	global_load_dword v110, v[130:131], off offset:-1024
	global_load_dword v111, v[130:131], off
	v_lshl_add_u64 v[132:133], v[130:131], 0, s[10:11]
	global_load_dwordx4 v[112:115], v[20:21], off offset:96
	global_load_dwordx4 v[116:119], v[20:21], off offset:112
	v_add_co_u32_e32 v138, vcc, 0xfffff000, v132
	s_nop 1
	v_addc_co_u32_e32 v139, vcc, -1, v133, vcc
	global_load_dword v120, v[138:139], off offset:-3072
	global_load_dword v121, v[138:139], off offset:-2048
	global_load_dword v122, v[138:139], off offset:-1024
	global_load_dword v123, v[132:133], off offset:-4096
	global_load_dword v124, v[132:133], off offset:-3072
	global_load_dword v125, v[132:133], off offset:-2048
	global_load_dword v126, v[132:133], off offset:-1024
	global_load_dword v127, v[132:133], off
	v_lshl_add_u64 v[8:9], v[132:133], 0, s[10:11]
	s_waitcnt vmcnt(0)
	v_fmac_f32_e32 v15, v64, v72
	v_fmac_f32_e32 v15, v65, v73
	v_fmac_f32_e32 v15, v66, v74
	v_fmac_f32_e32 v15, v67, v75
	v_fmac_f32_e32 v15, v68, v76
	v_fmac_f32_e32 v15, v69, v77
	v_fmac_f32_e32 v15, v70, v78
	v_fmac_f32_e32 v15, v71, v79
	v_fmac_f32_e32 v15, v80, v88
	v_fmac_f32_e32 v15, v81, v89
	v_fmac_f32_e32 v15, v82, v90
	v_fmac_f32_e32 v15, v83, v91
	v_fmac_f32_e32 v15, v84, v92
	v_fmac_f32_e32 v15, v85, v93
	v_fmac_f32_e32 v15, v86, v94
	v_fmac_f32_e32 v15, v87, v95
	v_fmac_f32_e32 v15, v96, v104
	v_fmac_f32_e32 v15, v97, v105
	v_fmac_f32_e32 v15, v98, v106
	v_fmac_f32_e32 v15, v99, v107
	v_fmac_f32_e32 v15, v100, v108
	v_fmac_f32_e32 v15, v101, v109
	v_fmac_f32_e32 v15, v102, v110
	v_fmac_f32_e32 v15, v103, v111
	v_fmac_f32_e32 v15, v112, v120
	v_fmac_f32_e32 v15, v113, v121
	v_fmac_f32_e32 v15, v114, v122
	v_fmac_f32_e32 v15, v115, v123
	v_fmac_f32_e32 v15, v116, v124
	v_fmac_f32_e32 v15, v117, v125
	v_fmac_f32_e32 v15, v118, v126
	v_fmac_f32_e32 v15, v119, v127
	s_cmpk_eq_i32 s12, 0x200
	s_cbranch_scc0 .LBB0_81
	ds_bpermute_b32 v6, v11, v15
	s_waitcnt lgkmcnt(0)
	v_add_f32_e32 v6, v15, v6
	ds_bpermute_b32 v7, v12, v6
	s_waitcnt lgkmcnt(0)
	v_add_f32_e32 v6, v6, v7
	ds_bpermute_b32 v7, v13, v6
	s_waitcnt lgkmcnt(0)
	v_add_f32_e32 v6, v6, v7
	ds_bpermute_b32 v7, v14, v6
	s_and_saveexec_b64 s[12:13], s[0:1]
	s_cbranch_execz .LBB0_79
	v_lshl_or_b32 v8, s14, 2, v1
	v_ashrrev_i32_e32 v9, 31, v8
	v_readlane_b32 s36, v253, 16
	v_lshlrev_b64 v[8:9], 2, v[8:9]
	v_readlane_b32 s38, v253, 18
	v_readlane_b32 s39, v253, 19
	s_waitcnt lgkmcnt(0)
	v_add_f32_e32 v6, v6, v7
	v_readlane_b32 s37, v253, 17
	v_lshl_add_u64 v[16:17], s[38:39], 0, v[8:9]
	global_load_dword v15, v[16:17], off
	v_lshl_add_u64 v[8:9], s[8:9], 0, v[8:9]
	v_readlane_b32 s40, v253, 20
	v_readlane_b32 s41, v253, 21
	v_readlane_b32 s42, v253, 22
	v_readlane_b32 s43, v253, 23
	v_readlane_b32 s44, v253, 24
	v_readlane_b32 s45, v253, 25
	v_readlane_b32 s46, v253, 26
	v_readlane_b32 s47, v253, 27
	v_readlane_b32 s48, v253, 28
	v_readlane_b32 s49, v253, 29
	v_readlane_b32 s50, v253, 30
	v_readlane_b32 s51, v253, 31
	s_waitcnt vmcnt(0)
	v_add_f32_e32 v6, v6, v15
	flat_store_dword v[8:9], v6 sc1
	s_branch .LBB0_79

; __device__ __forceinline__ void first_norm_row(const float* xrow, const float* g, bf16* urow, bf16* hrow, int lane) {
;     const f32x4* xp = (const f32x4*)xrow; const f32x4* gp = (const f32x4*)g;
;     f32x4 v[4] = {xp[2 * lane], xp[2 * lane + 1], xp[128 + 2 * lane], xp[128 + 2 * lane + 1]};
; __device__ __forceinline__ void prologue(const Ctx& C, const In& I, unsigned char* ws, bf16* hs0) {
;     ...
;     if (C.G == 256) { const int mb = 2048 * (C.bx & 7) + 64 * (C.bx >> 3) + 8 * C.wave;
;         for (int m = mb; m < mb + 8; ++m) first_norm_row(I.x + (size_t)m * D, I.norm_g, U + (size_t)m * D, hs0 + (size_t)m * D, C.lane); }
.LBB0_89:
	s_andn2_b64 vcc, exec, s[0:1]
	s_cbranch_vccnz .LBB0_92
	s_lshl_b32 s0, s18, 11
	s_and_b32 s1, s0, 0x3800
	s_and_b32 s0, s18, 0x1ffffff8
	s_add_i32 s0, s19, s0
	s_lshl_b32 s4, s18, 3
	s_lshl_b32 s0, s0, 3
	s_andn2_b32 s4, s4, 63
	s_add_i32 s0, s0, s1
	s_add_i32 s1, s1, s4
	s_lshl_b32 s4, s19, 3
	s_add_i32 s1, s1, s4
	s_add_i32 s9, s1, -1
	s_ashr_i32 s1, s0, 31
	s_or_b32 s8, s0, 7
	s_lshl_b64 s[4:5], s[0:1], 11
	s_add_u32 s2, s2, s4
	v_readlane_b32 s12, v253, 16
	s_addc_u32 s3, s3, s5
	v_readlane_b32 s26, v253, 30
	v_readlane_b32 s27, v253, 31
	s_add_u32 s4, s26, s4
	v_readlane_b32 s36, v253, 0
	s_addc_u32 s5, s27, s5
	s_lshl_b64 s[0:1], s[0:1], 12
	v_readlane_b32 s37, v253, 1
	s_add_u32 s0, s36, s0
	v_lshlrev_b32_e32 v2, 5, v1
	v_mov_b32_e32 v3, 0
	v_readlane_b32 s38, v253, 2
	v_readlane_b32 s39, v253, 3
	s_addc_u32 s1, s37, s1
	v_lshlrev_b32_e32 v20, 4, v1
	v_lshl_add_u64 v[18:19], s[38:39], 0, v[2:3]
	v_mov_b32_e32 v21, v3
	v_lshl_add_u64 v[22:23], s[0:1], 0, v[2:3]
	v_lshlrev_b32_e32 v64, 2, v2
	v_mov_b32_e32 v65, 0
	v_lshl_add_u64 v[64:65], s[0:1], 0, v[64:65]
	s_mov_b64 s[6:7], 0x2000
	s_mov_b64 s[10:11], 0x4000
	global_load_dword v72, v[64:65], off
	v_lshl_add_u64 v[66:67], v[64:65], 0, s[6:7]
	v_lshl_add_u64 v[68:69], v[64:65], 0, s[10:11]
	global_load_dword v73, v[66:67], off
	global_load_dword v74, v[68:69], off
	v_lshl_add_u64 v[70:71], v[68:69], 0, s[6:7]
	global_load_dword v75, v[70:71], off
	v_mov_b32_e32 v1, 0x358637bd
	s_mov_b32 s10, 0xf800000
	v_mov_b32_e32 v24, 0x260
	s_brev_b32 s11, 64
	s_mov_b32 s12, 0xb000000
	s_mov_b64 s[6:7], 0x1000
	v_readlane_b32 s40, v253, 4
	v_readlane_b32 s41, v253, 5
	v_readlane_b32 s42, v253, 6
	v_readlane_b32 s43, v253, 7
	v_readlane_b32 s44, v253, 8
	v_readlane_b32 s45, v253, 9
	v_readlane_b32 s46, v253, 10
	v_readlane_b32 s47, v253, 11
	v_readlane_b32 s48, v253, 12
	v_readlane_b32 s49, v253, 13
	v_readlane_b32 s50, v253, 14
	v_readlane_b32 s51, v253, 15
	v_readlane_b32 s13, v253, 17
	v_readlane_b32 s14, v253, 18
	v_readlane_b32 s15, v253, 19
	v_readlane_b32 s16, v253, 20
	v_readlane_b32 s17, v253, 21
	v_readlane_b32 s18, v253, 22
	v_readlane_b32 s19, v253, 23
	v_readlane_b32 s20, v253, 24
	v_readlane_b32 s21, v253, 25
	v_readlane_b32 s22, v253, 26
	v_readlane_b32 s23, v253, 27
	v_readlane_b32 s24, v253, 28
	v_readlane_b32 s25, v253, 29
